# attention: Q fragments fetched one query tile ahead
# baseline (speedup 1.0000x reference)
.LBB0_558:
	s_or_b64 exec, exec, s[10:11]
	s_waitcnt vmcnt(1)
	ds_write_b128 v81, v[2:5] offset:36864
	s_waitcnt vmcnt(0)
	ds_write_b128 v82, v[6:9] offset:36864
	v_lshlrev_b32_e32 v2, 2, v64
	v_lshl_or_b32 v2, s5, 4, v2
	s_waitcnt lgkmcnt(0)
	s_barrier
	global_load_dword v53, v2, s[6:7]
	s_lshr_b32 s5, s14, 4
	s_and_b32 s5, s5, 3
	s_lshl_b32 s10, s5, 9
	s_ashr_i32 s5, s4, 31
	s_and_b32 s8, s18, 0x780
	s_lshl_b64 s[4:5], s[4:5], 11
	v_or_b32_e32 v42, s8, v1
	v_mov_b32_e32 v3, s5
	v_or_b32_e32 v2, s4, v48
	v_lshl_add_u64 v[2:3], v[2:3], 0, v[42:43]
	v_lshlrev_b64 v[2:3], 11, v[2:3]
	v_or3_b32 v2, s10, v80, v2
	s_sub_i32 s8, 0x7f, s21
	v_lshl_add_u64 v[60:61], v[46:47], 0, v[2:3]
	v_lshl_add_u64 v[62:63], v[50:51], 0, v[2:3]
	s_mov_b64 s[10:11], 0
	v_mov_b32_e32 v42, v75
	v_mov_b32_e32 v55, v74
	v_lshl_add_u64 v[128:129], v[60:61], 0, s[10:11]
	v_add_co_u32_e32 v128, vcc, 0x3bc4a000, v128
	s_nop 1
	v_addc_co_u32_e32 v129, vcc, 0, v129, vcc
	global_load_dwordx4 v[120:123], v[128:129], off
	global_load_dwordx4 v[124:127], v[128:129], off offset:64
	global_load_dword v130, v[128:129], off
	global_load_dword v131, v[128:129], off
	global_load_dword v132, v[128:129], off
	global_load_dword v133, v[128:129], off
.LBB0_559:
	v_lshl_add_u64 v[2:3], v[60:61], 0, s[10:11]
	v_add_co_u32_e32 v6, vcc, 0x3bc4a000, v2
	v_min_u32_e32 v88, 6, v42
	s_nop 0
	v_addc_co_u32_e32 v7, vcc, 0, v3, vcc
	s_waitcnt vmcnt(4)
	v_mov_b32_e32 v2, v120
	v_mov_b32_e32 v3, v121
	v_mov_b32_e32 v4, v122
	v_mov_b32_e32 v5, v123
	v_mov_b32_e32 v90, v124
	v_mov_b32_e32 v91, v125
	v_mov_b32_e32 v92, v126
	v_mov_b32_e32 v93, v127
	v_add_co_u32_e32 v128, vcc, 0x8000, v6
	s_nop 1
	v_addc_co_u32_e32 v129, vcc, 0, v7, vcc
	global_load_dwordx4 v[120:123], v[128:129], off
	global_load_dwordx4 v[124:127], v[128:129], off offset:64
	v_lshlrev_b32_e32 v89, 4, v88
	v_or_b32_e32 v6, v89, v1
	v_mad_u32_u24 v10, v6, s17, v65
	ds_read_b128 v[6:9], v10
	ds_read_b128 v[10:13], v10 offset:64
	v_add_u32_e32 v98, 16, v89
	v_add_u32_e32 v87, 2, v88
	v_lshlrev_b32_e32 v99, 4, v87
	v_add_u32_e32 v100, 48, v89
	v_add_u32_e32 v86, 4, v88
	v_lshlrev_b32_e32 v101, 4, v86
	v_add_u32_e32 v102, 0x50, v89
	v_add_u32_e32 v59, 6, v88
	v_lshlrev_b32_e32 v103, 4, v59
	v_add_u32_e32 v104, 0x70, v89
	v_or_b32_e32 v57, 8, v88
	v_lshlrev_b32_e32 v105, 4, v57
	v_add_u32_e32 v106, 0x90, v89
	v_or_b32_e32 v89, v89, v66
	v_cmp_gt_u32_e32 vcc, v89, v55
	v_cmp_lt_i32_e64 s[4:5], s8, v89
	s_and_b64 vcc, vcc, s[4:5]
	v_cmp_le_i32_e64 s[4:5], s8, v89
	v_add_u32_e32 v42, 1, v42
	s_waitcnt lgkmcnt(1)
	v_mfma_f32_16x16x32_bf16 v[6:9], v[6:9], v[2:5], 0
	s_waitcnt lgkmcnt(0)
	v_mfma_f32_16x16x32_bf16 v[38:41], v[10:13], v[90:93], v[6:9]
	s_nop 5
	v_or_b32_e32 v6, v98, v1
	v_mad_u32_u24 v10, v6, s17, v65
	ds_read_b128 v[6:9], v10
	ds_read_b128 v[10:13], v10 offset:64
	s_waitcnt lgkmcnt(1)
	v_mfma_f32_16x16x32_bf16 v[6:9], v[6:9], v[2:5], 0
	v_cndmask_b32_e32 v38, v85, v38, vcc
	v_cmp_ge_u32_e32 vcc, v89, v55
	s_and_b64 vcc, vcc, s[4:5]
	s_waitcnt lgkmcnt(0)
	v_mfma_f32_16x16x32_bf16 v[34:37], v[10:13], v[90:93], v[6:9]
	v_cndmask_b32_e32 v39, v85, v39, vcc
	s_nop 1
	v_or_b32_e32 v6, v99, v1
	v_mad_u32_u24 v10, v6, s17, v65
	ds_read_b128 v[6:9], v10
	ds_read_b128 v[10:13], v10 offset:64
	s_waitcnt lgkmcnt(1)
	v_mfma_f32_16x16x32_bf16 v[6:9], v[6:9], v[2:5], 0
	s_waitcnt lgkmcnt(0)
	v_mfma_f32_16x16x32_bf16 v[30:33], v[10:13], v[90:93], v[6:9]
	s_nop 5
	v_or_b32_e32 v6, v100, v1
	v_mad_u32_u24 v10, v6, s17, v65
	ds_read_b128 v[6:9], v10
	ds_read_b128 v[10:13], v10 offset:64
	s_waitcnt lgkmcnt(1)
	v_mfma_f32_16x16x32_bf16 v[6:9], v[6:9], v[2:5], 0
	s_waitcnt lgkmcnt(0)
	v_mfma_f32_16x16x32_bf16 v[26:29], v[10:13], v[90:93], v[6:9]
	s_nop 5
	v_or_b32_e32 v6, v101, v1
	v_mad_u32_u24 v10, v6, s17, v65
	ds_read_b128 v[6:9], v10
	ds_read_b128 v[10:13], v10 offset:64
	s_waitcnt lgkmcnt(1)
	v_mfma_f32_16x16x32_bf16 v[6:9], v[6:9], v[2:5], 0
	s_waitcnt lgkmcnt(0)
	v_mfma_f32_16x16x32_bf16 v[22:25], v[10:13], v[90:93], v[6:9]
	s_nop 5
	v_or_b32_e32 v6, v102, v1
	v_mad_u32_u24 v10, v6, s17, v65
	ds_read_b128 v[6:9], v10
	ds_read_b128 v[10:13], v10 offset:64
	s_waitcnt lgkmcnt(1)
	v_mfma_f32_16x16x32_bf16 v[6:9], v[6:9], v[2:5], 0
	s_waitcnt lgkmcnt(0)
	v_mfma_f32_16x16x32_bf16 v[18:21], v[10:13], v[90:93], v[6:9]
	s_nop 5
	v_or_b32_e32 v6, v103, v1
	v_mad_u32_u24 v10, v6, s17, v65
	ds_read_b128 v[6:9], v10
	ds_read_b128 v[10:13], v10 offset:64
	s_waitcnt lgkmcnt(1)
	v_mfma_f32_16x16x32_bf16 v[6:9], v[6:9], v[2:5], 0
	s_waitcnt lgkmcnt(0)
	v_mfma_f32_16x16x32_bf16 v[14:17], v[10:13], v[90:93], v[6:9]
	s_nop 5
	v_or_b32_e32 v6, v104, v1
	v_mad_u32_u24 v10, v6, s17, v65
	ds_read_b128 v[6:9], v10
	ds_read_b128 v[10:13], v10 offset:64
	s_waitcnt lgkmcnt(1)
	v_mfma_f32_16x16x32_bf16 v[6:9], v[6:9], v[2:5], 0
	s_waitcnt lgkmcnt(0)
	v_mfma_f32_16x16x32_bf16 v[10:13], v[10:13], v[90:93], v[6:9]
	s_nop 5
	v_or_b32_e32 v6, v105, v1
	v_mad_u32_u24 v94, v6, s17, v65
	ds_read_b128 v[6:9], v94
	ds_read_b128 v[94:97], v94 offset:64
	s_waitcnt lgkmcnt(1)
	v_mfma_f32_16x16x32_bf16 v[6:9], v[6:9], v[2:5], 0
	s_waitcnt lgkmcnt(0)
	v_mfma_f32_16x16x32_bf16 v[6:9], v[94:97], v[90:93], v[6:9]
	v_or_b32_e32 v94, v106, v1
	v_mad_u32_u24 v107, v94, s17, v65
	ds_read_b128 v[94:97], v107
	s_waitcnt lgkmcnt(0)
	v_mfma_f32_16x16x32_bf16 v[2:5], v[94:97], v[2:5], 0
	ds_read_b128 v[94:97], v107 offset:64
	s_waitcnt lgkmcnt(0)
	v_mfma_f32_16x16x32_bf16 v[2:5], v[94:97], v[90:93], v[2:5]
	v_or_b32_e32 v92, 2, v89
	v_cmp_gt_u32_e32 vcc, v92, v55
	v_cmp_lt_i32_e64 s[4:5], s8, v92
	s_and_b64 vcc, vcc, s[4:5]
	v_or_b32_e32 v89, 3, v89
	v_cndmask_b32_e32 v40, v85, v40, vcc
	v_cmp_gt_u32_e32 vcc, v89, v55
	v_cmp_lt_i32_e64 s[4:5], s8, v89
	s_and_b64 vcc, vcc, s[4:5]
	v_max3_f32 v91, v38, s20, v39
	v_cndmask_b32_e32 v41, v85, v41, vcc
	v_max3_f32 v89, v91, v40, v41
	v_or_b32_e32 v91, v98, v66
	v_cmp_gt_u32_e32 vcc, v91, v55
	v_cmp_lt_i32_e64 s[4:5], s8, v91
	s_and_b64 vcc, vcc, s[4:5]
	v_cndmask_b32_e32 v34, v85, v34, vcc
	v_cmp_ge_u32_e32 vcc, v91, v55
	v_cmp_le_i32_e64 s[4:5], s8, v91
	s_and_b64 vcc, vcc, s[4:5]
	v_or_b32_e32 v92, 2, v91
	v_cndmask_b32_e32 v35, v85, v35, vcc
	v_cmp_gt_u32_e32 vcc, v92, v55
	v_cmp_lt_i32_e64 s[4:5], s8, v92
	s_and_b64 vcc, vcc, s[4:5]
	v_or_b32_e32 v91, 3, v91
	v_cndmask_b32_e32 v36, v85, v36, vcc
	v_cmp_gt_u32_e32 vcc, v91, v55
	v_cmp_lt_i32_e64 s[4:5], s8, v91
	s_and_b64 vcc, vcc, s[4:5]
	v_or_b32_e32 v91, v99, v66
	v_cndmask_b32_e32 v37, v85, v37, vcc
	v_cmp_gt_u32_e32 vcc, v91, v55
	v_cmp_lt_i32_e64 s[4:5], s8, v91
	s_and_b64 vcc, vcc, s[4:5]
	v_cndmask_b32_e32 v30, v85, v30, vcc
	v_cmp_ge_u32_e32 vcc, v91, v55
	v_cmp_le_i32_e64 s[4:5], s8, v91
	s_and_b64 vcc, vcc, s[4:5]
	v_or_b32_e32 v92, 2, v91
	v_cndmask_b32_e32 v31, v85, v31, vcc
	v_cmp_gt_u32_e32 vcc, v92, v55
	v_cmp_lt_i32_e64 s[4:5], s8, v92
	s_and_b64 vcc, vcc, s[4:5]
	v_or_b32_e32 v91, 3, v91
	v_cndmask_b32_e32 v32, v85, v32, vcc
	v_cmp_gt_u32_e32 vcc, v91, v55
	v_cmp_lt_i32_e64 s[4:5], s8, v91
	v_add_u32_e32 v90, 0x80, v55
	s_and_b64 vcc, vcc, s[4:5]
	v_or_b32_e32 v91, v100, v66
	v_cndmask_b32_e32 v33, v85, v33, vcc
	v_cmp_gt_u32_e32 vcc, v91, v55
	v_cmp_le_u32_e64 s[4:5], v91, v90
	s_and_b64 s[4:5], vcc, s[4:5]
	v_cmp_lt_i32_e32 vcc, s8, v91
	s_and_b64 vcc, s[4:5], vcc
	v_cmp_lt_u32_e64 s[4:5], v91, v90
	v_cndmask_b32_e32 v26, v85, v26, vcc
	v_cmp_ge_u32_e32 vcc, v91, v55
	s_and_b64 s[4:5], vcc, s[4:5]
	v_cmp_le_i32_e32 vcc, s8, v91
	s_and_b64 vcc, s[4:5], vcc
	v_or_b32_e32 v92, 2, v91
	v_cndmask_b32_e32 v27, v85, v27, vcc
	v_cmp_gt_u32_e32 vcc, v92, v55
	v_cmp_le_u32_e64 s[4:5], v92, v90
	s_and_b64 s[4:5], vcc, s[4:5]
	v_cmp_lt_i32_e32 vcc, s8, v92
	s_and_b64 vcc, s[4:5], vcc
	v_or_b32_e32 v91, 3, v91
	v_cndmask_b32_e32 v28, v85, v28, vcc
	v_cmp_gt_u32_e32 vcc, v91, v55
	v_cmp_le_u32_e64 s[4:5], v91, v90
	s_and_b64 s[4:5], vcc, s[4:5]
	v_cmp_lt_i32_e32 vcc, s8, v91
	s_and_b64 vcc, s[4:5], vcc
	v_or_b32_e32 v91, v101, v66
	v_cndmask_b32_e32 v29, v85, v29, vcc
	v_cmp_gt_u32_e32 vcc, v91, v55
	v_cmp_le_u32_e64 s[4:5], v91, v90
	s_and_b64 s[4:5], vcc, s[4:5]
	v_cmp_lt_i32_e32 vcc, s8, v91
	s_and_b64 vcc, s[4:5], vcc
	v_cmp_lt_u32_e64 s[4:5], v91, v90
	v_cndmask_b32_e32 v22, v85, v22, vcc
	v_cmp_ge_u32_e32 vcc, v91, v55
	s_and_b64 s[4:5], vcc, s[4:5]
	v_cmp_le_i32_e32 vcc, s8, v91
	s_and_b64 vcc, s[4:5], vcc
	v_or_b32_e32 v92, 2, v91
	v_cndmask_b32_e32 v23, v85, v23, vcc
	v_cmp_gt_u32_e32 vcc, v92, v55
	v_cmp_le_u32_e64 s[4:5], v92, v90
	s_and_b64 s[4:5], vcc, s[4:5]
	v_cmp_lt_i32_e32 vcc, s8, v92
	s_and_b64 vcc, s[4:5], vcc
	v_or_b32_e32 v91, 3, v91
	v_cndmask_b32_e32 v24, v85, v24, vcc
	v_cmp_gt_u32_e32 vcc, v91, v55
	v_cmp_le_u32_e64 s[4:5], v91, v90
	s_and_b64 s[4:5], vcc, s[4:5]
	v_cmp_lt_i32_e32 vcc, s8, v91
	s_and_b64 vcc, s[4:5], vcc
	v_or_b32_e32 v91, v102, v66
	v_cndmask_b32_e32 v25, v85, v25, vcc
	v_cmp_gt_u32_e32 vcc, v91, v55
	v_cmp_le_u32_e64 s[4:5], v91, v90
	s_and_b64 s[4:5], vcc, s[4:5]
	v_cmp_lt_i32_e32 vcc, s8, v91
	s_and_b64 vcc, s[4:5], vcc
	v_cmp_lt_u32_e64 s[4:5], v91, v90
	v_cndmask_b32_e32 v18, v85, v18, vcc
	v_cmp_ge_u32_e32 vcc, v91, v55
	s_and_b64 s[4:5], vcc, s[4:5]
	v_cmp_le_i32_e32 vcc, s8, v91
	s_and_b64 vcc, s[4:5], vcc
	v_or_b32_e32 v92, 2, v91
	v_cndmask_b32_e32 v19, v85, v19, vcc
	v_cmp_gt_u32_e32 vcc, v92, v55
	v_cmp_le_u32_e64 s[4:5], v92, v90
	s_and_b64 s[4:5], vcc, s[4:5]
	v_cmp_lt_i32_e32 vcc, s8, v92
	s_and_b64 vcc, s[4:5], vcc
	v_or_b32_e32 v91, 3, v91
	v_cndmask_b32_e32 v20, v85, v20, vcc
	v_cmp_gt_u32_e32 vcc, v91, v55
	v_cmp_le_u32_e64 s[4:5], v91, v90
	s_and_b64 s[4:5], vcc, s[4:5]
	v_cmp_lt_i32_e32 vcc, s8, v91
	s_and_b64 vcc, s[4:5], vcc
	v_or_b32_e32 v91, v103, v66
	v_cndmask_b32_e32 v21, v85, v21, vcc
	v_cmp_gt_u32_e32 vcc, v91, v55
	v_cmp_le_u32_e64 s[4:5], v91, v90
	s_and_b64 s[4:5], vcc, s[4:5]
	v_cmp_lt_i32_e32 vcc, s8, v91
	s_and_b64 vcc, s[4:5], vcc
	v_cmp_lt_u32_e64 s[4:5], v91, v90
	v_cndmask_b32_e32 v14, v85, v14, vcc
	v_cmp_ge_u32_e32 vcc, v91, v55
	s_and_b64 s[4:5], vcc, s[4:5]
	v_cmp_le_i32_e32 vcc, s8, v91
	s_and_b64 vcc, s[4:5], vcc
	v_or_b32_e32 v92, 2, v91
	v_cndmask_b32_e32 v15, v85, v15, vcc
	v_cmp_gt_u32_e32 vcc, v92, v55
	v_cmp_le_u32_e64 s[4:5], v92, v90
	s_and_b64 s[4:5], vcc, s[4:5]
	v_cmp_lt_i32_e32 vcc, s8, v92
	s_and_b64 vcc, s[4:5], vcc
	v_or_b32_e32 v91, 3, v91
	v_cndmask_b32_e32 v16, v85, v16, vcc
	v_cmp_gt_u32_e32 vcc, v91, v55
	v_cmp_le_u32_e64 s[4:5], v91, v90
	s_and_b64 s[4:5], vcc, s[4:5]
	v_cmp_lt_i32_e32 vcc, s8, v91
	s_and_b64 vcc, s[4:5], vcc
	v_or_b32_e32 v91, v104, v66
	v_cndmask_b32_e32 v17, v85, v17, vcc
	v_cmp_gt_u32_e32 vcc, v91, v55
	v_cmp_le_u32_e64 s[4:5], v91, v90
	s_and_b64 s[4:5], vcc, s[4:5]
	v_cmp_lt_i32_e32 vcc, s8, v91
	s_and_b64 vcc, s[4:5], vcc
	v_cmp_lt_u32_e64 s[4:5], v91, v90
	v_cndmask_b32_e32 v10, v85, v10, vcc
	v_cmp_ge_u32_e32 vcc, v91, v55
	v_max3_f32 v89, v89, v34, v35
	s_and_b64 s[4:5], vcc, s[4:5]
	v_cmp_le_i32_e32 vcc, s8, v91
	v_max3_f32 v89, v89, v36, v37
	s_and_b64 vcc, s[4:5], vcc
	v_or_b32_e32 v92, 2, v91
	v_max3_f32 v89, v89, v30, v31
	v_cndmask_b32_e32 v11, v85, v11, vcc
	v_cmp_gt_u32_e32 vcc, v92, v55
	v_cmp_le_u32_e64 s[4:5], v92, v90
	v_max3_f32 v89, v89, v32, v33
	s_and_b64 s[4:5], vcc, s[4:5]
	v_cmp_lt_i32_e32 vcc, s8, v92
	v_max3_f32 v89, v89, v26, v27
	s_and_b64 vcc, s[4:5], vcc
	v_or_b32_e32 v91, 3, v91
	v_max3_f32 v89, v89, v28, v29
	v_cndmask_b32_e32 v12, v85, v12, vcc
	v_cmp_gt_u32_e32 vcc, v91, v55
	v_cmp_le_u32_e64 s[4:5], v91, v90
	v_max3_f32 v89, v89, v22, v23
	s_and_b64 s[4:5], vcc, s[4:5]
	v_cmp_lt_i32_e32 vcc, s8, v91
	v_max3_f32 v89, v89, v24, v25
	s_and_b64 vcc, s[4:5], vcc
	v_or_b32_e32 v91, v105, v66
	v_max3_f32 v89, v89, v18, v19
	v_cndmask_b32_e32 v13, v85, v13, vcc
	v_cmp_le_u32_e32 vcc, v91, v90
	v_max3_f32 v89, v89, v20, v21
	v_or_b32_e32 v92, 2, v91
	v_cndmask_b32_e32 v6, v85, v6, vcc
	v_cmp_lt_u32_e32 vcc, v91, v90
	v_max3_f32 v89, v89, v14, v15
	v_or_b32_e32 v91, 3, v91
	v_cndmask_b32_e32 v7, v85, v7, vcc
	v_cmp_le_u32_e32 vcc, v92, v90
	v_max3_f32 v89, v89, v16, v17
	v_max3_f32 v89, v89, v10, v11
	v_cndmask_b32_e32 v8, v85, v8, vcc
	v_cmp_le_u32_e32 vcc, v91, v90
	v_or_b32_e32 v91, v106, v66
	v_max3_f32 v89, v89, v12, v13
	v_cndmask_b32_e32 v9, v85, v9, vcc
	v_cmp_le_u32_e32 vcc, v91, v90
	v_or_b32_e32 v92, 2, v91
	v_max3_f32 v89, v89, v6, v7
	v_cndmask_b32_e32 v2, v85, v2, vcc
	v_cmp_lt_u32_e32 vcc, v91, v90
	v_or_b32_e32 v91, 3, v91
	v_max3_f32 v89, v89, v8, v9
	v_cndmask_b32_e32 v3, v85, v3, vcc
	v_cmp_le_u32_e32 vcc, v92, v90
	v_max3_f32 v89, v89, v2, v3
	v_add_u32_e32 v55, 16, v55
	v_cndmask_b32_e32 v4, v85, v4, vcc
	v_cmp_le_u32_e32 vcc, v91, v90
	s_nop 1
	v_cndmask_b32_e32 v5, v85, v5, vcc
	v_max3_f32 v89, v89, v4, v5
	ds_bpermute_b32 v90, v67, v89
	s_waitcnt lgkmcnt(0)
	v_max_f32_e32 v90, v90, v90
	v_max_f32_e32 v89, v89, v90
	ds_bpermute_b32 v90, v68, v89
	s_waitcnt lgkmcnt(0)
	v_max3_f32 v89, v89, v90, v53
	v_sub_f32_e32 v38, v38, v89
	v_mul_f32_e32 v38, 0x3fb8aa3b, v38
	v_sub_f32_e32 v39, v39, v89
	v_exp_f32_e32 v38, v38
	v_mul_f32_e32 v39, 0x3fb8aa3b, v39
	v_sub_f32_e32 v40, v40, v89
	v_exp_f32_e32 v39, v39
	v_mul_f32_e32 v40, 0x3fb8aa3b, v40
	v_sub_f32_e32 v41, v41, v89
	v_exp_f32_e32 v40, v40
	v_mul_f32_e32 v41, 0x3fb8aa3b, v41
	v_sub_f32_e32 v34, v34, v89
	v_exp_f32_e32 v41, v41
	v_mul_f32_e32 v34, 0x3fb8aa3b, v34
	v_sub_f32_e32 v35, v35, v89
	v_add_f32_e32 v90, 0, v38
	v_exp_f32_e32 v34, v34
	v_mul_f32_e32 v35, 0x3fb8aa3b, v35
	v_sub_f32_e32 v36, v36, v89
	v_add_f32_e32 v90, v39, v90
	v_exp_f32_e32 v35, v35
	v_mul_f32_e32 v36, 0x3fb8aa3b, v36
	v_sub_f32_e32 v37, v37, v89
	v_add_f32_e32 v90, v40, v90
	v_exp_f32_e32 v36, v36
	v_mul_f32_e32 v37, 0x3fb8aa3b, v37
	v_sub_f32_e32 v30, v30, v89
	v_add_f32_e32 v90, v41, v90
	v_exp_f32_e32 v37, v37
	v_mul_f32_e32 v30, 0x3fb8aa3b, v30
	v_sub_f32_e32 v31, v31, v89
	v_add_f32_e32 v90, v34, v90
	v_exp_f32_e32 v30, v30
	v_mul_f32_e32 v31, 0x3fb8aa3b, v31
	v_sub_f32_e32 v32, v32, v89
	v_add_f32_e32 v90, v35, v90
	v_exp_f32_e32 v31, v31
	v_mul_f32_e32 v32, 0x3fb8aa3b, v32
	v_sub_f32_e32 v33, v33, v89
	v_add_f32_e32 v90, v36, v90
	v_exp_f32_e32 v32, v32
	v_mul_f32_e32 v33, 0x3fb8aa3b, v33
	v_sub_f32_e32 v26, v26, v89
	v_add_f32_e32 v90, v37, v90
	v_exp_f32_e32 v33, v33
	v_mul_f32_e32 v26, 0x3fb8aa3b, v26
	v_sub_f32_e32 v27, v27, v89
	v_add_f32_e32 v90, v30, v90
	v_exp_f32_e32 v26, v26
	v_mul_f32_e32 v27, 0x3fb8aa3b, v27
	v_sub_f32_e32 v28, v28, v89
	v_add_f32_e32 v90, v31, v90
	v_exp_f32_e32 v27, v27
	v_mul_f32_e32 v28, 0x3fb8aa3b, v28
	v_sub_f32_e32 v29, v29, v89
	v_add_f32_e32 v90, v32, v90
	v_exp_f32_e32 v28, v28
	v_mul_f32_e32 v29, 0x3fb8aa3b, v29
	v_sub_f32_e32 v22, v22, v89
	v_add_f32_e32 v90, v33, v90
	v_exp_f32_e32 v29, v29
	v_mul_f32_e32 v22, 0x3fb8aa3b, v22
	v_add_f32_e32 v90, v26, v90
	v_exp_f32_e32 v91, v22
	v_add_f32_e32 v90, v27, v90
	v_add_f32_e32 v90, v28, v90
	v_sub_f32_e32 v23, v23, v89
	v_add_f32_e32 v90, v29, v90
	v_mul_f32_e32 v23, 0x3fb8aa3b, v23
	v_add_f32_e32 v22, v91, v90
	v_exp_f32_e32 v90, v23
	v_sub_f32_e32 v23, v24, v89
	v_mul_f32_e32 v23, 0x3fb8aa3b, v23
	v_exp_f32_e32 v92, v23
	v_sub_f32_e32 v23, v25, v89
	v_sub_f32_e32 v19, v19, v89
	v_mul_f32_e32 v23, 0x3fb8aa3b, v23
	v_sub_f32_e32 v18, v18, v89
	v_mul_f32_e32 v19, 0x3fb8aa3b, v19
	v_exp_f32_e32 v93, v23
	v_mul_f32_e32 v18, 0x3fb8aa3b, v18
	v_exp_f32_e32 v95, v19
	v_sub_f32_e32 v19, v20, v89
	v_exp_f32_e32 v94, v18
	v_mul_f32_e32 v19, 0x3fb8aa3b, v19
	v_add_f32_e32 v22, v90, v22
	v_exp_f32_e32 v96, v19
	v_sub_f32_e32 v19, v21, v89
	v_sub_f32_e32 v15, v15, v89
	v_add_f32_e32 v22, v92, v22
	v_mul_f32_e32 v19, 0x3fb8aa3b, v19
	v_sub_f32_e32 v14, v14, v89
	v_mul_f32_e32 v15, 0x3fb8aa3b, v15
	v_add_f32_e32 v22, v93, v22
	v_exp_f32_e32 v97, v19
	v_mul_f32_e32 v14, 0x3fb8aa3b, v14
	v_exp_f32_e32 v99, v15
	v_sub_f32_e32 v15, v16, v89
	v_add_f32_e32 v18, v94, v22
	v_exp_f32_e32 v98, v14
	v_mul_f32_e32 v15, 0x3fb8aa3b, v15
	v_add_f32_e32 v18, v95, v18
	v_exp_f32_e32 v100, v15
	v_sub_f32_e32 v15, v17, v89
	v_sub_f32_e32 v11, v11, v89
	v_add_f32_e32 v18, v96, v18
	v_mul_f32_e32 v15, 0x3fb8aa3b, v15
	v_sub_f32_e32 v10, v10, v89
	v_mul_f32_e32 v11, 0x3fb8aa3b, v11
	v_add_f32_e32 v18, v97, v18
	v_exp_f32_e32 v101, v15
	v_mul_f32_e32 v10, 0x3fb8aa3b, v10
	v_exp_f32_e32 v103, v11
	v_sub_f32_e32 v11, v12, v89
	v_add_f32_e32 v14, v98, v18
	v_exp_f32_e32 v102, v10
	v_mul_f32_e32 v11, 0x3fb8aa3b, v11
	v_add_f32_e32 v14, v99, v14
	v_exp_f32_e32 v104, v11
	v_sub_f32_e32 v11, v13, v89
	v_sub_f32_e32 v7, v7, v89
	v_add_f32_e32 v14, v100, v14
	v_mul_f32_e32 v11, 0x3fb8aa3b, v11
	v_sub_f32_e32 v6, v6, v89
	v_mul_f32_e32 v7, 0x3fb8aa3b, v7
	v_add_f32_e32 v14, v101, v14
	v_exp_f32_e32 v105, v11
	v_mul_f32_e32 v6, 0x3fb8aa3b, v6
	v_exp_f32_e32 v107, v7
	v_sub_f32_e32 v7, v8, v89
	v_add_f32_e32 v10, v102, v14
	v_exp_f32_e32 v106, v6
	v_mul_f32_e32 v7, 0x3fb8aa3b, v7
	v_add_f32_e32 v10, v103, v10
	v_exp_f32_e32 v108, v7
	v_sub_f32_e32 v7, v9, v89
	v_sub_f32_e32 v3, v3, v89
	v_add_f32_e32 v10, v104, v10
	v_mul_f32_e32 v7, 0x3fb8aa3b, v7
	v_sub_f32_e32 v2, v2, v89
	v_mul_f32_e32 v3, 0x3fb8aa3b, v3
	v_add_f32_e32 v10, v105, v10
	v_exp_f32_e32 v109, v7
	v_mul_f32_e32 v2, 0x3fb8aa3b, v2
	v_exp_f32_e32 v111, v3
	v_sub_f32_e32 v3, v4, v89
	v_add_f32_e32 v6, v106, v10
	v_exp_f32_e32 v110, v2
	v_mul_f32_e32 v3, 0x3fb8aa3b, v3
	v_add_f32_e32 v6, v107, v6
	v_exp_f32_e32 v112, v3
	v_sub_f32_e32 v3, v5, v89
	v_add_f32_e32 v6, v108, v6
	v_mul_f32_e32 v3, 0x3fb8aa3b, v3
	v_add_f32_e32 v6, v109, v6
	v_exp_f32_e32 v113, v3
	v_add_f32_e32 v2, v110, v6
	v_add_f32_e32 v2, v111, v2
	v_add_f32_e32 v2, v112, v2
	v_add_f32_e32 v2, v113, v2
	ds_bpermute_b32 v3, v67, v2
	v_lshl_add_u32 v18, v88, 5, v73
	v_add_u32_e32 v10, 0xb000, v18
	v_add_u32_e32 v14, 0xd000, v18
	s_waitcnt lgkmcnt(0)
	v_add_f32_e32 v2, v2, v3
	ds_bpermute_b32 v3, v68, v2
	s_waitcnt lgkmcnt(0)
	v_add_f32_e32 v2, v2, v3
	v_sub_f32_e32 v3, v53, v89
	v_mul_f32_e32 v3, 0x3fb8aa3b, v3
	v_exp_f32_e32 v3, v3
	s_nop 0
	v_add_f32_e32 v2, v3, v2
	v_div_scale_f32 v3, s[4:5], v2, v2, 1.0
	v_rcp_f32_e32 v4, v3
	s_nop 0
	v_fma_f32 v5, -v3, v4, 1.0
	v_fmac_f32_e32 v4, v5, v4
	v_div_scale_f32 v5, vcc, 1.0, v2, 1.0
	v_mul_f32_e32 v6, v5, v4
	v_fma_f32 v7, -v3, v6, v5
	v_fmac_f32_e32 v6, v7, v4
	v_fma_f32 v3, -v3, v6, v5
	v_div_fmas_f32 v3, v3, v4, v6
	v_div_fixup_f32 v89, v3, v2, 1.0
	v_mul_f32_e32 v2, v38, v89
	v_mul_f32_e32 v3, v39, v89
	v_cvt_pk_bf16_f32 v2, v2, v3
	v_mul_f32_e32 v3, v40, v89
	v_mul_f32_e32 v4, v41, v89
	v_cvt_pk_bf16_f32 v3, v3, v4
	v_mul_f32_e32 v4, v34, v89
	v_mul_f32_e32 v5, v35, v89
	v_cvt_pk_bf16_f32 v4, v4, v5
	v_mul_f32_e32 v5, v36, v89
	v_mul_f32_e32 v6, v37, v89
	v_cvt_pk_bf16_f32 v5, v5, v6
	v_add_u32_e32 v6, 0x9000, v18
	v_add_u32_e32 v18, 0xf000, v18
	ds_read2_b64 v[6:9], v6 offset1:4
	ds_read2_b64 v[10:13], v10 offset0:32 offset1:36
	ds_read2_b64 v[14:17], v14 offset0:64 offset1:68
	ds_read2_b64 v[18:21], v18 offset0:96 offset1:100
	s_waitcnt lgkmcnt(3)
	v_mfma_f32_16x16x32_bf16 v[6:9], v[6:9], v[2:5], 0
	v_mul_f32_e32 v22, v29, v89
	s_waitcnt lgkmcnt(2)
	v_mfma_f32_16x16x32_bf16 v[10:13], v[10:13], v[2:5], 0
	s_waitcnt lgkmcnt(1)
	v_mfma_f32_16x16x32_bf16 v[14:17], v[14:17], v[2:5], 0
	s_waitcnt lgkmcnt(0)
	v_mfma_f32_16x16x32_bf16 v[2:5], v[18:21], v[2:5], 0
	v_mul_f32_e32 v18, v30, v89
	v_mul_f32_e32 v19, v31, v89
	v_cvt_pk_bf16_f32 v18, v18, v19
	v_mul_f32_e32 v19, v32, v89
	v_mul_f32_e32 v20, v33, v89
	v_cvt_pk_bf16_f32 v19, v19, v20
	v_mul_f32_e32 v20, v26, v89
	v_mul_f32_e32 v21, v27, v89
	v_cvt_pk_bf16_f32 v20, v20, v21
	v_mul_f32_e32 v21, v28, v89
	v_lshl_add_u32 v26, v87, 5, v73
	v_cvt_pk_bf16_f32 v21, v21, v22
	v_add_u32_e32 v22, 0x9000, v26
	ds_read2_b64 v[22:25], v22 offset1:4
	s_waitcnt lgkmcnt(0)
	v_mfma_f32_16x16x32_bf16 v[6:9], v[22:25], v[18:21], v[6:9]
	v_add_u32_e32 v22, 0xb000, v26
	ds_read2_b64 v[22:25], v22 offset0:32 offset1:36
	s_waitcnt lgkmcnt(0)
	v_mfma_f32_16x16x32_bf16 v[10:13], v[22:25], v[18:21], v[10:13]
	v_add_u32_e32 v22, 0xd000, v26
	ds_read2_b64 v[22:25], v22 offset0:64 offset1:68
	s_waitcnt lgkmcnt(0)
	v_mfma_f32_16x16x32_bf16 v[14:17], v[22:25], v[18:21], v[14:17]
	v_add_u32_e32 v22, 0xf000, v26
	ds_read2_b64 v[22:25], v22 offset0:96 offset1:100
	v_lshl_add_u32 v26, v86, 5, v73
	s_waitcnt lgkmcnt(0)
	v_mfma_f32_16x16x32_bf16 v[2:5], v[22:25], v[18:21], v[2:5]
	v_mul_f32_e32 v18, v91, v89
	v_mul_f32_e32 v19, v90, v89
	v_cvt_pk_bf16_f32 v18, v18, v19
	v_mul_f32_e32 v19, v92, v89
	v_mul_f32_e32 v20, v93, v89
	v_cvt_pk_bf16_f32 v19, v19, v20
	v_mul_f32_e32 v20, v94, v89
	v_mul_f32_e32 v21, v95, v89
	v_cvt_pk_bf16_f32 v20, v20, v21
	v_mul_f32_e32 v21, v96, v89
	v_mul_f32_e32 v22, v97, v89
	v_cvt_pk_bf16_f32 v21, v21, v22
	v_add_u32_e32 v22, 0x9000, v26
	ds_read2_b64 v[22:25], v22 offset1:4
	s_waitcnt lgkmcnt(0)
	v_mfma_f32_16x16x32_bf16 v[6:9], v[22:25], v[18:21], v[6:9]
	v_add_u32_e32 v22, 0xb000, v26
	ds_read2_b64 v[22:25], v22 offset0:32 offset1:36
	s_waitcnt lgkmcnt(0)
	v_mfma_f32_16x16x32_bf16 v[10:13], v[22:25], v[18:21], v[10:13]
	v_add_u32_e32 v22, 0xd000, v26
	ds_read2_b64 v[22:25], v22 offset0:64 offset1:68
	s_waitcnt lgkmcnt(0)
	v_mfma_f32_16x16x32_bf16 v[14:17], v[22:25], v[18:21], v[14:17]
	v_add_u32_e32 v22, 0xf000, v26
	ds_read2_b64 v[22:25], v22 offset0:96 offset1:100
	v_lshl_add_u32 v26, v59, 5, v73
	s_waitcnt lgkmcnt(0)
	v_mfma_f32_16x16x32_bf16 v[2:5], v[22:25], v[18:21], v[2:5]
	v_mul_f32_e32 v18, v98, v89
	v_mul_f32_e32 v19, v99, v89
	v_cvt_pk_bf16_f32 v18, v18, v19
	v_mul_f32_e32 v19, v100, v89
	v_mul_f32_e32 v20, v101, v89
	v_cvt_pk_bf16_f32 v19, v19, v20
	v_mul_f32_e32 v20, v102, v89
	v_mul_f32_e32 v21, v103, v89
	v_cvt_pk_bf16_f32 v20, v20, v21
	v_mul_f32_e32 v21, v104, v89
	v_mul_f32_e32 v22, v105, v89
	v_cvt_pk_bf16_f32 v21, v21, v22
	v_add_u32_e32 v22, 0x9000, v26
	ds_read2_b64 v[22:25], v22 offset1:4
	s_waitcnt lgkmcnt(0)
	v_mfma_f32_16x16x32_bf16 v[6:9], v[22:25], v[18:21], v[6:9]
	v_add_u32_e32 v22, 0xb000, v26
	ds_read2_b64 v[22:25], v22 offset0:32 offset1:36
	s_waitcnt lgkmcnt(0)
	v_mfma_f32_16x16x32_bf16 v[10:13], v[22:25], v[18:21], v[10:13]
	v_add_u32_e32 v22, 0xd000, v26
	ds_read2_b64 v[22:25], v22 offset0:64 offset1:68
	s_waitcnt lgkmcnt(0)
	v_mfma_f32_16x16x32_bf16 v[14:17], v[22:25], v[18:21], v[14:17]
	v_add_u32_e32 v22, 0xf000, v26
	ds_read2_b64 v[22:25], v22 offset0:96 offset1:100
	v_lshl_add_u32 v26, v57, 5, v73
	s_waitcnt lgkmcnt(0)
	v_mfma_f32_16x16x32_bf16 v[18:21], v[22:25], v[18:21], v[2:5]
	s_nop 2
	v_mul_f32_e32 v2, v106, v89
	v_mul_f32_e32 v3, v107, v89
	v_cvt_pk_bf16_f32 v22, v2, v3
	v_mul_f32_e32 v2, v108, v89
	v_mul_f32_e32 v3, v109, v89
	v_cvt_pk_bf16_f32 v23, v2, v3
	v_mul_f32_e32 v2, v110, v89
	v_mul_f32_e32 v3, v111, v89
	v_cvt_pk_bf16_f32 v24, v2, v3
	v_mul_f32_e32 v2, v112, v89
	v_mul_f32_e32 v3, v113, v89
	v_cvt_pk_bf16_f32 v25, v2, v3
	v_add_u32_e32 v2, 0x9000, v26
	ds_read2_b64 v[2:5], v2 offset1:4
	s_waitcnt lgkmcnt(0)
	v_mfma_f32_16x16x32_bf16 v[2:5], v[2:5], v[22:25], v[6:9]
	s_nop 2
	v_add_u32_e32 v6, 0xb000, v26
	ds_read2_b64 v[6:9], v6 offset0:32 offset1:36
	s_nop 2
	v_cvt_pk_bf16_f32 v2, v2, v3
	s_waitcnt lgkmcnt(0)
	v_mfma_f32_16x16x32_bf16 v[6:9], v[6:9], v[22:25], v[10:13]
	s_nop 2
	v_add_u32_e32 v10, 0xd000, v26
	ds_read2_b64 v[10:13], v10 offset0:64 offset1:68
	v_cvt_pk_bf16_f32 v3, v4, v5
	s_waitcnt lgkmcnt(0)
	v_mfma_f32_16x16x32_bf16 v[10:13], v[10:13], v[22:25], v[14:17]
	s_nop 2
	v_add_u32_e32 v14, 0xf000, v26
	ds_read2_b64 v[14:17], v14 offset0:96 offset1:100
	s_waitcnt lgkmcnt(0)
	v_mfma_f32_16x16x32_bf16 v[14:17], v[14:17], v[22:25], v[18:21]
	s_nop 2
	v_lshl_add_u64 v[18:19], v[62:63], 0, s[10:11]
	global_store_dwordx2 v[18:19], v[2:3], off offset:-64
	v_cvt_pk_bf16_f32 v2, v6, v7
	v_cvt_pk_bf16_f32 v3, v8, v9
	s_add_u32 s10, s10, 0x8000
	global_store_dwordx2 v[18:19], v[2:3], off offset:-32
	v_cvt_pk_bf16_f32 v2, v10, v11
	v_cvt_pk_bf16_f32 v3, v12, v13
	s_addc_u32 s11, s11, 0
	global_store_dwordx2 v[18:19], v[2:3], off
	v_cvt_pk_bf16_f32 v2, v14, v15
	v_cvt_pk_bf16_f32 v3, v16, v17
	s_cmp_eq_u32 s10, 0x20000
	global_store_dwordx2 v[18:19], v[2:3], off offset:32
	s_cbranch_scc0 .LBB0_559
	s_add_i32 s14, s14, s3
	s_add_i32 s18, s18, s19
	s_cmpk_gt_i32 s14, 0x1ff
	s_cbranch_scc0 .LBB0_549
